# static priority placement: s_setprio 0 moved from before the back-edge counter block to just behind the loop-back barrier in the six K-loops
# speedup vs baseline: 1.0015x; 1.0015x over previous
.LBB0_285:
	ds_read_b128 v[18:21], v201
	ds_read_b128 v[22:25], v201 offset:1024
	ds_read_b128 v[26:29], v201 offset:2048
	ds_read_b128 v[30:33], v201 offset:3072
	ds_read_b128 v[2:5], v202
	ds_read_b128 v[6:9], v202 offset:1024
	ds_read_b128 v[10:13], v202 offset:2048
	ds_read_b128 v[14:17], v202 offset:3072
	s_add_u32 s62, s58, 0xfffc0080
	s_addc_u32 s63, s59, -1
	s_cmp_eq_u32 s71, 12
	s_cselect_b32 s67, s43, s63
	s_cselect_b32 s66, s57, s62
	s_cselect_b32 s63, s45, s70
	s_cselect_b32 s62, s68, s69
	v_lshl_add_u64 v[232:233], s[58:59], 0, v[172:173]
	s_add_i32 m0, s55, 0xc000
	ds_read_b128 v[176:179], v203
	ds_read_b128 v[180:183], v203 offset:1024
	ds_read_b128 v[206:209], v203 offset:2048
	ds_read_b128 v[210:213], v203 offset:3072
	ds_read_b128 v[214:217], v203 offset:4096
	ds_read_b128 v[218:221], v203 offset:5120
	ds_read_b128 v[222:225], v203 offset:6144
	ds_read_b128 v[226:229], v203 offset:7168
	global_load_lds_dwordx4 v[232:233], off
	v_lshl_add_u64 v[232:233], s[58:59], 0, v[174:175]
	s_add_i32 m0, s55, 0xe000
	s_nop 0
	global_load_lds_dwordx4 v[232:233], off
	s_waitcnt vmcnt(8)
	s_waitcnt lgkmcnt(0)
	s_barrier
	s_setprio 1
	s_waitcnt lgkmcnt(0)
	v_mfma_scale_f32_16x16x128_f8f6f4 v[158:161], v[18:25], v[176:183], v[158:161], v204, v204 op_sel_hi:[0,0,0]
	v_mfma_scale_f32_16x16x128_f8f6f4 v[154:157], v[26:33], v[176:183], v[154:157], v204, v204 op_sel_hi:[0,0,0]
	v_mfma_scale_f32_16x16x128_f8f6f4 v[150:153], v[18:25], v[206:213], v[150:153], v204, v204 op_sel_hi:[0,0,0]
	v_mfma_scale_f32_16x16x128_f8f6f4 v[146:149], v[26:33], v[206:213], v[146:149], v204, v204 op_sel_hi:[0,0,0]
	v_mfma_scale_f32_16x16x128_f8f6f4 v[130:133], v[18:25], v[214:221], v[130:133], v204, v204 op_sel_hi:[0,0,0]
	v_mfma_scale_f32_16x16x128_f8f6f4 v[122:125], v[26:33], v[214:221], v[122:125], v204, v204 op_sel_hi:[0,0,0]
	v_mfma_scale_f32_16x16x128_f8f6f4 v[118:121], v[18:25], v[222:229], v[118:121], v204, v204 op_sel_hi:[0,0,0]
	v_mfma_scale_f32_16x16x128_f8f6f4 v[114:117], v[26:33], v[222:229], v[114:117], v204, v204 op_sel_hi:[0,0,0]
	s_setprio 0
	s_setprio 1
	v_mfma_scale_f32_16x16x128_f8f6f4 v[142:145], v[2:9], v[176:183], v[142:145], v204, v204 op_sel_hi:[0,0,0]
	v_mfma_scale_f32_16x16x128_f8f6f4 v[138:141], v[10:17], v[176:183], v[138:141], v204, v204 op_sel_hi:[0,0,0]
	v_mfma_scale_f32_16x16x128_f8f6f4 v[134:137], v[2:9], v[206:213], v[134:137], v204, v204 op_sel_hi:[0,0,0]
	v_mfma_scale_f32_16x16x128_f8f6f4 v[126:129], v[10:17], v[206:213], v[126:129], v204, v204 op_sel_hi:[0,0,0]
	v_mfma_scale_f32_16x16x128_f8f6f4 v[110:113], v[2:9], v[214:221], v[110:113], v204, v204 op_sel_hi:[0,0,0]
	v_mfma_scale_f32_16x16x128_f8f6f4 v[106:109], v[10:17], v[214:221], v[106:109], v204, v204 op_sel_hi:[0,0,0]
	v_mfma_scale_f32_16x16x128_f8f6f4 v[102:105], v[2:9], v[222:229], v[102:105], v204, v204 op_sel_hi:[0,0,0]
	v_mfma_scale_f32_16x16x128_f8f6f4 v[98:101], v[10:17], v[222:229], v[98:101], v204, v204 op_sel_hi:[0,0,0]
	s_setprio 0
	s_barrier
	s_add_i32 vcc_lo, s97, s39
	v_lshl_add_u64 v[176:177], s[62:63], 0, v[164:165]
	s_mov_b32 m0, vcc_lo
	ds_read_b128 v[206:209], v203 offset:16384
	ds_read_b128 v[210:213], v203 offset:17408
	ds_read_b128 v[214:217], v203 offset:18432
	ds_read_b128 v[218:221], v203 offset:19456
	ds_read_b128 v[222:225], v203 offset:20480
	ds_read_b128 v[226:229], v203 offset:21504
	ds_read_b128 v[232:235], v203 offset:22528
	ds_read_b128 v[236:239], v203 offset:23552
	global_load_lds_dwordx4 v[176:177], off
	s_add_i32 m0, vcc_lo, 0x2000
	s_add_u32 vcc_lo, s62, 0x40000
	v_lshl_add_u64 v[178:179], s[62:63], 0, v[168:169]
	s_addc_u32 vcc_hi, s63, 0
	s_add_i32 s18, s34, s39
	global_load_lds_dwordx4 v[178:179], off
	v_lshl_add_u64 v[180:181], vcc, 0, v[164:165]
	s_mov_b32 m0, s18
	v_lshl_add_u64 v[182:183], s[66:67], 0, v[166:167]
	global_load_lds_dwordx4 v[180:181], off
	v_lshl_add_u64 v[180:181], vcc, 0, v[168:169]
	s_add_i32 m0, s18, 0x2000
	s_nop 0
	global_load_lds_dwordx4 v[180:181], off
	v_lshl_add_u64 v[180:181], s[66:67], 0, v[162:163]
	s_mov_b32 m0, s55
	s_nop 0
	global_load_lds_dwordx4 v[180:181], off
	s_mov_b32 m0, s90
	s_nop 0
	global_load_lds_dwordx4 v[182:183], off
	s_waitcnt vmcnt(8)
	s_waitcnt lgkmcnt(0)
	s_barrier
	s_setprio 1
	s_waitcnt lgkmcnt(0)
	v_mfma_scale_f32_16x16x128_f8f6f4 v[94:97], v[18:25], v[206:213], v[94:97], v204, v204 op_sel_hi:[0,0,0]
	v_mfma_scale_f32_16x16x128_f8f6f4 v[90:93], v[26:33], v[206:213], v[90:93], v204, v204 op_sel_hi:[0,0,0]
	v_mfma_scale_f32_16x16x128_f8f6f4 v[86:89], v[18:25], v[214:221], v[86:89], v204, v204 op_sel_hi:[0,0,0]
	v_mfma_scale_f32_16x16x128_f8f6f4 v[82:85], v[26:33], v[214:221], v[82:85], v204, v204 op_sel_hi:[0,0,0]
	v_mfma_scale_f32_16x16x128_f8f6f4 v[66:69], v[18:25], v[222:229], v[66:69], v204, v204 op_sel_hi:[0,0,0]
	v_mfma_scale_f32_16x16x128_f8f6f4 v[58:61], v[26:33], v[222:229], v[58:61], v204, v204 op_sel_hi:[0,0,0]
	v_mfma_scale_f32_16x16x128_f8f6f4 v[54:57], v[18:25], v[232:239], v[54:57], v204, v204 op_sel_hi:[0,0,0]
	v_mfma_scale_f32_16x16x128_f8f6f4 v[50:53], v[26:33], v[232:239], v[50:53], v204, v204 op_sel_hi:[0,0,0]
	s_setprio 0
	s_setprio 1
	v_mfma_scale_f32_16x16x128_f8f6f4 v[78:81], v[2:9], v[206:213], v[78:81], v204, v204 op_sel_hi:[0,0,0]
	v_mfma_scale_f32_16x16x128_f8f6f4 v[74:77], v[10:17], v[206:213], v[74:77], v204, v204 op_sel_hi:[0,0,0]
	v_mfma_scale_f32_16x16x128_f8f6f4 v[70:73], v[2:9], v[214:221], v[70:73], v204, v204 op_sel_hi:[0,0,0]
	v_mfma_scale_f32_16x16x128_f8f6f4 v[62:65], v[10:17], v[214:221], v[62:65], v204, v204 op_sel_hi:[0,0,0]
	v_mfma_scale_f32_16x16x128_f8f6f4 v[46:49], v[2:9], v[222:229], v[46:49], v204, v204 op_sel_hi:[0,0,0]
	v_mfma_scale_f32_16x16x128_f8f6f4 v[42:45], v[10:17], v[222:229], v[42:45], v204, v204 op_sel_hi:[0,0,0]
	v_mfma_scale_f32_16x16x128_f8f6f4 v[38:41], v[2:9], v[232:239], v[38:41], v204, v204 op_sel_hi:[0,0,0]
	v_mfma_scale_f32_16x16x128_f8f6f4 v[34:37], v[10:17], v[232:239], v[34:37], v204, v204 op_sel_hi:[0,0,0]
	s_setprio 0
	s_barrier
	s_add_i32 s18, 0, 0x18000
	s_add_i32 s19, 0, 0x1c000
	v_add_u32_e32 v14, s18, v198
	v_add_u32_e32 v30, s19, v198
	ds_read_b128 v[2:5], v14
	ds_read_b128 v[6:9], v14 offset:1024
	ds_read_b128 v[10:13], v14 offset:2048
	ds_read_b128 v[14:17], v14 offset:3072
	ds_read_b128 v[18:21], v30
	ds_read_b128 v[22:25], v30 offset:1024
	ds_read_b128 v[26:29], v30 offset:2048
	ds_read_b128 v[30:33], v30 offset:3072
	s_add_u32 s66, s66, 0x40000
	s_addc_u32 s67, s67, 0
	s_mov_b32 m0, s91
	v_lshl_add_u64 v[240:241], s[66:67], 0, v[162:163]
	ds_read_b128 v[206:209], v203 offset:32768
	ds_read_b128 v[210:213], v203 offset:33792
	ds_read_b128 v[214:217], v203 offset:34816
	ds_read_b128 v[218:221], v203 offset:35840
	ds_read_b128 v[222:225], v203 offset:36864
	ds_read_b128 v[226:229], v203 offset:37888
	ds_read_b128 v[232:235], v203 offset:38912
	ds_read_b128 v[236:239], v203 offset:39936
	global_load_lds_dwordx4 v[240:241], off
	v_lshl_add_u64 v[240:241], s[66:67], 0, v[166:167]
	s_mov_b32 m0, s92
	s_nop 0
	global_load_lds_dwordx4 v[240:241], off
	s_waitcnt vmcnt(8)
	s_waitcnt lgkmcnt(0)
	s_barrier
	s_setprio 1
	s_waitcnt lgkmcnt(0)
	v_mfma_scale_f32_16x16x128_f8f6f4 v[158:161], v[2:9], v[206:213], v[158:161], v204, v204 op_sel_hi:[0,0,0]
	v_mfma_scale_f32_16x16x128_f8f6f4 v[154:157], v[10:17], v[206:213], v[154:157], v204, v204 op_sel_hi:[0,0,0]
	v_mfma_scale_f32_16x16x128_f8f6f4 v[150:153], v[2:9], v[214:221], v[150:153], v204, v204 op_sel_hi:[0,0,0]
	v_mfma_scale_f32_16x16x128_f8f6f4 v[146:149], v[10:17], v[214:221], v[146:149], v204, v204 op_sel_hi:[0,0,0]
	v_mfma_scale_f32_16x16x128_f8f6f4 v[130:133], v[2:9], v[222:229], v[130:133], v204, v204 op_sel_hi:[0,0,0]
	v_mfma_scale_f32_16x16x128_f8f6f4 v[122:125], v[10:17], v[222:229], v[122:125], v204, v204 op_sel_hi:[0,0,0]
	v_mfma_scale_f32_16x16x128_f8f6f4 v[118:121], v[2:9], v[232:239], v[118:121], v204, v204 op_sel_hi:[0,0,0]
	v_mfma_scale_f32_16x16x128_f8f6f4 v[114:117], v[10:17], v[232:239], v[114:117], v204, v204 op_sel_hi:[0,0,0]
	s_setprio 0
	s_setprio 1
	v_mfma_scale_f32_16x16x128_f8f6f4 v[142:145], v[18:25], v[206:213], v[142:145], v204, v204 op_sel_hi:[0,0,0]
	v_mfma_scale_f32_16x16x128_f8f6f4 v[138:141], v[26:33], v[206:213], v[138:141], v204, v204 op_sel_hi:[0,0,0]
	v_mfma_scale_f32_16x16x128_f8f6f4 v[134:137], v[18:25], v[214:221], v[134:137], v204, v204 op_sel_hi:[0,0,0]
	v_mfma_scale_f32_16x16x128_f8f6f4 v[126:129], v[26:33], v[214:221], v[126:129], v204, v204 op_sel_hi:[0,0,0]
	v_mfma_scale_f32_16x16x128_f8f6f4 v[110:113], v[18:25], v[222:229], v[110:113], v204, v204 op_sel_hi:[0,0,0]
	v_mfma_scale_f32_16x16x128_f8f6f4 v[106:109], v[26:33], v[222:229], v[106:109], v204, v204 op_sel_hi:[0,0,0]
	v_mfma_scale_f32_16x16x128_f8f6f4 v[102:105], v[18:25], v[232:239], v[102:105], v204, v204 op_sel_hi:[0,0,0]
	v_mfma_scale_f32_16x16x128_f8f6f4 v[98:101], v[26:33], v[232:239], v[98:101], v204, v204 op_sel_hi:[0,0,0]
	s_setprio 0
	s_barrier
	s_add_i32 s18, s18, s39
	v_lshl_add_u64 v[176:177], v[176:177], 0, s[14:15]
	s_mov_b32 m0, s18
	ds_read_b128 v[206:209], v203 offset:49152
	ds_read_b128 v[210:213], v203 offset:50176
	ds_read_b128 v[214:217], v203 offset:51200
	ds_read_b128 v[218:221], v203 offset:52224
	ds_read_b128 v[222:225], v203 offset:53248
	ds_read_b128 v[226:229], v203 offset:54272
	ds_read_b128 v[232:235], v203 offset:55296
	ds_read_b128 v[236:239], v203 offset:56320
	global_load_lds_dwordx4 v[176:177], off
	s_add_i32 m0, s18, 0x2000
	s_add_u32 s62, s62, 0x40080
	v_lshl_add_u64 v[176:177], v[178:179], 0, s[14:15]
	s_addc_u32 s63, s63, 0
	s_add_i32 s18, s19, s39
	global_load_lds_dwordx4 v[176:177], off
	v_lshl_add_u64 v[176:177], s[62:63], 0, v[164:165]
	s_mov_b32 m0, s18
	s_nop 0
	global_load_lds_dwordx4 v[176:177], off
	v_lshl_add_u64 v[176:177], s[62:63], 0, v[168:169]
	s_add_i32 m0, s18, 0x2000
	s_nop 0
	global_load_lds_dwordx4 v[176:177], off
	v_lshl_add_u64 v[176:177], v[180:181], 0, s[14:15]
	s_mov_b32 m0, s93
	s_nop 0
	global_load_lds_dwordx4 v[176:177], off
	v_lshl_add_u64 v[176:177], v[182:183], 0, s[14:15]
	s_mov_b32 m0, s95
	s_nop 0
	global_load_lds_dwordx4 v[176:177], off
	s_waitcnt vmcnt(8)
	s_waitcnt lgkmcnt(0)
	s_barrier
	s_setprio 1
	s_waitcnt lgkmcnt(0)
	v_mfma_scale_f32_16x16x128_f8f6f4 v[94:97], v[2:9], v[206:213], v[94:97], v204, v204 op_sel_hi:[0,0,0]
	v_mfma_scale_f32_16x16x128_f8f6f4 v[90:93], v[10:17], v[206:213], v[90:93], v204, v204 op_sel_hi:[0,0,0]
	v_mfma_scale_f32_16x16x128_f8f6f4 v[86:89], v[2:9], v[214:221], v[86:89], v204, v204 op_sel_hi:[0,0,0]
	v_mfma_scale_f32_16x16x128_f8f6f4 v[82:85], v[10:17], v[214:221], v[82:85], v204, v204 op_sel_hi:[0,0,0]
	v_mfma_scale_f32_16x16x128_f8f6f4 v[66:69], v[2:9], v[222:229], v[66:69], v204, v204 op_sel_hi:[0,0,0]
	v_mfma_scale_f32_16x16x128_f8f6f4 v[58:61], v[10:17], v[222:229], v[58:61], v204, v204 op_sel_hi:[0,0,0]
	v_mfma_scale_f32_16x16x128_f8f6f4 v[54:57], v[2:9], v[232:239], v[54:57], v204, v204 op_sel_hi:[0,0,0]
	v_mfma_scale_f32_16x16x128_f8f6f4 v[50:53], v[10:17], v[232:239], v[50:53], v204, v204 op_sel_hi:[0,0,0]
	s_setprio 0
	s_setprio 1
	v_mfma_scale_f32_16x16x128_f8f6f4 v[78:81], v[18:25], v[206:213], v[78:81], v204, v204 op_sel_hi:[0,0,0]
	v_mfma_scale_f32_16x16x128_f8f6f4 v[74:77], v[26:33], v[206:213], v[74:77], v204, v204 op_sel_hi:[0,0,0]
	v_mfma_scale_f32_16x16x128_f8f6f4 v[70:73], v[18:25], v[214:221], v[70:73], v204, v204 op_sel_hi:[0,0,0]
	v_mfma_scale_f32_16x16x128_f8f6f4 v[62:65], v[26:33], v[214:221], v[62:65], v204, v204 op_sel_hi:[0,0,0]
	v_mfma_scale_f32_16x16x128_f8f6f4 v[46:49], v[18:25], v[222:229], v[46:49], v204, v204 op_sel_hi:[0,0,0]
	v_mfma_scale_f32_16x16x128_f8f6f4 v[42:45], v[26:33], v[222:229], v[42:45], v204, v204 op_sel_hi:[0,0,0]
	v_mfma_scale_f32_16x16x128_f8f6f4 v[38:41], v[18:25], v[232:239], v[38:41], v204, v204 op_sel_hi:[0,0,0]
	v_mfma_scale_f32_16x16x128_f8f6f4 v[34:37], v[26:33], v[232:239], v[34:37], v204, v204 op_sel_hi:[0,0,0]
	s_add_i32 s71, s71, 2
	s_add_u32 s58, s58, 0x100
	s_addc_u32 s59, s59, 0
	s_add_u32 s69, s69, 0x100
	s_addc_u32 s70, s70, 0
	s_cmp_gt_u32 s71, 13
	s_barrier
	s_setprio 0
	s_cbranch_scc0 .LBB0_285
	s_and_b64 vcc, exec, s[16:17]
	s_cbranch_vccz .LBB0_288
	s_barrier

.LBB0_336:
	ds_read_b128 v[142:145], v1
	ds_read_b128 v[152:155], v1 offset:1024
	ds_read_b128 v[156:159], v1 offset:2048
	ds_read_b128 v[160:163], v1 offset:3072
	ds_read_b128 v[164:167], v149
	ds_read_b128 v[168:171], v149 offset:1024
	ds_read_b128 v[172:175], v149 offset:2048
	ds_read_b128 v[176:179], v149 offset:3072
	s_add_u32 s18, s48, 0xfff80080
	s_addc_u32 s19, s49, -1
	s_cmp_eq_u32 s87, 28
	s_cselect_b32 s55, s17, s19
	s_cselect_b32 s54, s56, s18
	s_cselect_b32 s53, s39, s59
	s_cselect_b32 s52, s57, s58
	v_lshl_add_u64 v[212:213], s[48:49], 0, v[138:139]
	s_add_i32 m0, s47, 0xc000
	ds_read_b128 v[180:183], v150
	ds_read_b128 v[184:187], v150 offset:1024
	ds_read_b128 v[188:191], v150 offset:2048
	ds_read_b128 v[192:195], v150 offset:3072
	ds_read_b128 v[196:199], v150 offset:4096
	ds_read_b128 v[200:203], v150 offset:5120
	ds_read_b128 v[204:207], v150 offset:6144
	ds_read_b128 v[208:211], v150 offset:7168
	global_load_lds_dwordx4 v[212:213], off
	v_lshl_add_u64 v[212:213], s[48:49], 0, v[140:141]
	s_add_i32 m0, s47, 0xe000
	s_nop 0
	global_load_lds_dwordx4 v[212:213], off
	s_waitcnt vmcnt(8)
	s_waitcnt lgkmcnt(0)
	s_barrier
	s_setprio 1
	s_waitcnt lgkmcnt(0)
	v_mfma_f32_16x16x32_bf16 v[126:129], v[142:145], v[180:183], v[126:129]
	v_mfma_f32_16x16x32_bf16 v[122:125], v[156:159], v[180:183], v[122:125]
	v_mfma_f32_16x16x32_bf16 v[114:117], v[142:145], v[188:191], v[114:117]
	v_mfma_f32_16x16x32_bf16 v[106:109], v[156:159], v[188:191], v[106:109]
	v_mfma_f32_16x16x32_bf16 v[98:101], v[142:145], v[196:199], v[98:101]
	v_mfma_f32_16x16x32_bf16 v[90:93], v[156:159], v[196:199], v[90:93]
	v_mfma_f32_16x16x32_bf16 v[82:85], v[142:145], v[204:207], v[82:85]
	v_mfma_f32_16x16x32_bf16 v[74:77], v[156:159], v[204:207], v[74:77]
	v_mfma_f32_16x16x32_bf16 v[126:129], v[152:155], v[184:187], v[126:129]
	v_mfma_f32_16x16x32_bf16 v[122:125], v[160:163], v[184:187], v[122:125]
	v_mfma_f32_16x16x32_bf16 v[114:117], v[152:155], v[192:195], v[114:117]
	v_mfma_f32_16x16x32_bf16 v[106:109], v[160:163], v[192:195], v[106:109]
	v_mfma_f32_16x16x32_bf16 v[98:101], v[152:155], v[200:203], v[98:101]
	v_mfma_f32_16x16x32_bf16 v[90:93], v[160:163], v[200:203], v[90:93]
	v_mfma_f32_16x16x32_bf16 v[82:85], v[152:155], v[208:211], v[82:85]
	v_mfma_f32_16x16x32_bf16 v[74:77], v[160:163], v[208:211], v[74:77]
	s_setprio 0
	s_setprio 1
	v_mfma_f32_16x16x32_bf16 v[118:121], v[164:167], v[180:183], v[118:121]
	v_mfma_f32_16x16x32_bf16 v[110:113], v[172:175], v[180:183], v[110:113]
	v_mfma_f32_16x16x32_bf16 v[102:105], v[164:167], v[188:191], v[102:105]
	v_mfma_f32_16x16x32_bf16 v[94:97], v[172:175], v[188:191], v[94:97]
	v_mfma_f32_16x16x32_bf16 v[86:89], v[164:167], v[196:199], v[86:89]
	v_mfma_f32_16x16x32_bf16 v[78:81], v[172:175], v[196:199], v[78:81]
	v_mfma_f32_16x16x32_bf16 v[70:73], v[164:167], v[204:207], v[70:73]
	v_mfma_f32_16x16x32_bf16 v[66:69], v[172:175], v[204:207], v[66:69]
	v_mfma_f32_16x16x32_bf16 v[118:121], v[168:171], v[184:187], v[118:121]
	v_mfma_f32_16x16x32_bf16 v[110:113], v[176:179], v[184:187], v[110:113]
	v_mfma_f32_16x16x32_bf16 v[102:105], v[168:171], v[192:195], v[102:105]
	v_mfma_f32_16x16x32_bf16 v[94:97], v[176:179], v[192:195], v[94:97]
	v_mfma_f32_16x16x32_bf16 v[86:89], v[168:171], v[200:203], v[86:89]
	v_mfma_f32_16x16x32_bf16 v[78:81], v[176:179], v[200:203], v[78:81]
	v_mfma_f32_16x16x32_bf16 v[70:73], v[168:171], v[208:211], v[70:73]
	v_mfma_f32_16x16x32_bf16 v[66:69], v[176:179], v[208:211], v[66:69]
	s_setprio 0
	s_barrier
	s_add_i32 s18, s71, s30
	v_lshl_add_u64 v[212:213], s[52:53], 0, v[132:133]
	s_mov_b32 m0, s18
	ds_read_b128 v[180:183], v150 offset:16384
	ds_read_b128 v[184:187], v150 offset:17408
	ds_read_b128 v[188:191], v150 offset:18432
	ds_read_b128 v[192:195], v150 offset:19456
	ds_read_b128 v[196:199], v150 offset:20480
	ds_read_b128 v[200:203], v150 offset:21504
	ds_read_b128 v[204:207], v150 offset:22528
	ds_read_b128 v[208:211], v150 offset:23552
	global_load_lds_dwordx4 v[212:213], off
	s_add_i32 m0, s18, 0x2000
	s_add_u32 s90, s52, 0x80000
	v_lshl_add_u64 v[214:215], s[52:53], 0, v[136:137]
	s_addc_u32 s91, s53, 0
	s_add_i32 s18, s84, s30
	global_load_lds_dwordx4 v[214:215], off
	v_lshl_add_u64 v[216:217], s[90:91], 0, v[132:133]
	s_mov_b32 m0, s18
	v_lshl_add_u64 v[218:219], s[54:55], 0, v[134:135]
	global_load_lds_dwordx4 v[216:217], off
	v_lshl_add_u64 v[216:217], s[90:91], 0, v[136:137]
	s_add_i32 m0, s18, 0x2000
	s_nop 0
	global_load_lds_dwordx4 v[216:217], off
	v_lshl_add_u64 v[216:217], s[54:55], 0, v[130:131]
	s_mov_b32 m0, s47
	s_nop 0
	global_load_lds_dwordx4 v[216:217], off
	s_mov_b32 m0, s63
	s_nop 0
	global_load_lds_dwordx4 v[218:219], off
	s_waitcnt vmcnt(8)
	s_waitcnt lgkmcnt(0)
	s_barrier
	s_setprio 1
	s_waitcnt lgkmcnt(0)
	v_mfma_f32_16x16x32_bf16 v[62:65], v[142:145], v[180:183], v[62:65]
	v_mfma_f32_16x16x32_bf16 v[58:61], v[156:159], v[180:183], v[58:61]
	v_mfma_f32_16x16x32_bf16 v[50:53], v[142:145], v[188:191], v[50:53]
	v_mfma_f32_16x16x32_bf16 v[42:45], v[156:159], v[188:191], v[42:45]
	v_mfma_f32_16x16x32_bf16 v[34:37], v[142:145], v[196:199], v[34:37]
	v_mfma_f32_16x16x32_bf16 v[26:29], v[156:159], v[196:199], v[26:29]
	v_mfma_f32_16x16x32_bf16 v[18:21], v[142:145], v[204:207], v[18:21]
	v_mfma_f32_16x16x32_bf16 v[10:13], v[156:159], v[204:207], v[10:13]
	v_mfma_f32_16x16x32_bf16 v[62:65], v[152:155], v[184:187], v[62:65]
	v_mfma_f32_16x16x32_bf16 v[58:61], v[160:163], v[184:187], v[58:61]
	v_mfma_f32_16x16x32_bf16 v[50:53], v[152:155], v[192:195], v[50:53]
	v_mfma_f32_16x16x32_bf16 v[42:45], v[160:163], v[192:195], v[42:45]
	v_mfma_f32_16x16x32_bf16 v[34:37], v[152:155], v[200:203], v[34:37]
	v_mfma_f32_16x16x32_bf16 v[26:29], v[160:163], v[200:203], v[26:29]
	v_mfma_f32_16x16x32_bf16 v[18:21], v[152:155], v[208:211], v[18:21]
	v_mfma_f32_16x16x32_bf16 v[10:13], v[160:163], v[208:211], v[10:13]
	s_setprio 0
	s_setprio 1
	v_mfma_f32_16x16x32_bf16 v[54:57], v[164:167], v[180:183], v[54:57]
	v_mfma_f32_16x16x32_bf16 v[46:49], v[172:175], v[180:183], v[46:49]
	v_mfma_f32_16x16x32_bf16 v[38:41], v[164:167], v[188:191], v[38:41]
	v_mfma_f32_16x16x32_bf16 v[30:33], v[172:175], v[188:191], v[30:33]
	v_mfma_f32_16x16x32_bf16 v[22:25], v[164:167], v[196:199], v[22:25]
	v_mfma_f32_16x16x32_bf16 v[14:17], v[172:175], v[196:199], v[14:17]
	v_mfma_f32_16x16x32_bf16 v[6:9], v[164:167], v[204:207], v[6:9]
	v_mfma_f32_16x16x32_bf16 v[2:5], v[172:175], v[204:207], v[2:5]
	v_mfma_f32_16x16x32_bf16 v[54:57], v[168:171], v[184:187], v[54:57]
	v_mfma_f32_16x16x32_bf16 v[46:49], v[176:179], v[184:187], v[46:49]
	v_mfma_f32_16x16x32_bf16 v[38:41], v[168:171], v[192:195], v[38:41]
	v_mfma_f32_16x16x32_bf16 v[30:33], v[176:179], v[192:195], v[30:33]
	v_mfma_f32_16x16x32_bf16 v[22:25], v[168:171], v[200:203], v[22:25]
	v_mfma_f32_16x16x32_bf16 v[14:17], v[176:179], v[200:203], v[14:17]
	v_mfma_f32_16x16x32_bf16 v[6:9], v[168:171], v[208:211], v[6:9]
	v_mfma_f32_16x16x32_bf16 v[2:5], v[176:179], v[208:211], v[2:5]
	s_setprio 0
	s_barrier
	s_add_i32 s18, 0, 0x18000
	v_add_u32_e32 v151, s18, v147
	s_add_i32 s19, 0, 0x1c000
	ds_read_b128 v[142:145], v151
	ds_read_b128 v[152:155], v151 offset:1024
	ds_read_b128 v[156:159], v151 offset:2048
	ds_read_b128 v[160:163], v151 offset:3072
	v_add_u32_e32 v151, s19, v147
	ds_read_b128 v[164:167], v151
	ds_read_b128 v[168:171], v151 offset:1024
	ds_read_b128 v[172:175], v151 offset:2048
	ds_read_b128 v[176:179], v151 offset:3072
	s_add_u32 s54, s54, 0x80000
	s_addc_u32 s55, s55, 0
	s_mov_b32 m0, s66
	v_lshl_add_u64 v[220:221], s[54:55], 0, v[130:131]
	ds_read_b128 v[180:183], v150 offset:32768
	ds_read_b128 v[184:187], v150 offset:33792
	ds_read_b128 v[188:191], v150 offset:34816
	ds_read_b128 v[192:195], v150 offset:35840
	ds_read_b128 v[196:199], v150 offset:36864
	ds_read_b128 v[200:203], v150 offset:37888
	ds_read_b128 v[204:207], v150 offset:38912
	ds_read_b128 v[208:211], v150 offset:39936
	global_load_lds_dwordx4 v[220:221], off
	v_lshl_add_u64 v[220:221], s[54:55], 0, v[134:135]
	s_mov_b32 m0, s67
	s_nop 0
	global_load_lds_dwordx4 v[220:221], off
	s_waitcnt vmcnt(8)
	s_waitcnt lgkmcnt(0)
	s_barrier
	s_setprio 1
	s_waitcnt lgkmcnt(0)
	v_mfma_f32_16x16x32_bf16 v[126:129], v[142:145], v[180:183], v[126:129]
	v_mfma_f32_16x16x32_bf16 v[122:125], v[156:159], v[180:183], v[122:125]
	v_mfma_f32_16x16x32_bf16 v[114:117], v[142:145], v[188:191], v[114:117]
	v_mfma_f32_16x16x32_bf16 v[106:109], v[156:159], v[188:191], v[106:109]
	v_mfma_f32_16x16x32_bf16 v[98:101], v[142:145], v[196:199], v[98:101]
	v_mfma_f32_16x16x32_bf16 v[90:93], v[156:159], v[196:199], v[90:93]
	v_mfma_f32_16x16x32_bf16 v[82:85], v[142:145], v[204:207], v[82:85]
	v_mfma_f32_16x16x32_bf16 v[74:77], v[156:159], v[204:207], v[74:77]
	v_mfma_f32_16x16x32_bf16 v[126:129], v[152:155], v[184:187], v[126:129]
	v_mfma_f32_16x16x32_bf16 v[122:125], v[160:163], v[184:187], v[122:125]
	v_mfma_f32_16x16x32_bf16 v[114:117], v[152:155], v[192:195], v[114:117]
	v_mfma_f32_16x16x32_bf16 v[106:109], v[160:163], v[192:195], v[106:109]
	v_mfma_f32_16x16x32_bf16 v[98:101], v[152:155], v[200:203], v[98:101]
	v_mfma_f32_16x16x32_bf16 v[90:93], v[160:163], v[200:203], v[90:93]
	v_mfma_f32_16x16x32_bf16 v[82:85], v[152:155], v[208:211], v[82:85]
	v_mfma_f32_16x16x32_bf16 v[74:77], v[160:163], v[208:211], v[74:77]
	s_setprio 0
	s_setprio 1
	v_mfma_f32_16x16x32_bf16 v[118:121], v[164:167], v[180:183], v[118:121]
	v_mfma_f32_16x16x32_bf16 v[110:113], v[172:175], v[180:183], v[110:113]
	v_mfma_f32_16x16x32_bf16 v[102:105], v[164:167], v[188:191], v[102:105]
	v_mfma_f32_16x16x32_bf16 v[94:97], v[172:175], v[188:191], v[94:97]
	v_mfma_f32_16x16x32_bf16 v[86:89], v[164:167], v[196:199], v[86:89]
	v_mfma_f32_16x16x32_bf16 v[78:81], v[172:175], v[196:199], v[78:81]
	v_mfma_f32_16x16x32_bf16 v[70:73], v[164:167], v[204:207], v[70:73]
	v_mfma_f32_16x16x32_bf16 v[66:69], v[172:175], v[204:207], v[66:69]
	v_mfma_f32_16x16x32_bf16 v[118:121], v[168:171], v[184:187], v[118:121]
	v_mfma_f32_16x16x32_bf16 v[110:113], v[176:179], v[184:187], v[110:113]
	v_mfma_f32_16x16x32_bf16 v[102:105], v[168:171], v[192:195], v[102:105]
	v_mfma_f32_16x16x32_bf16 v[94:97], v[176:179], v[192:195], v[94:97]
	v_mfma_f32_16x16x32_bf16 v[86:89], v[168:171], v[200:203], v[86:89]
	v_mfma_f32_16x16x32_bf16 v[78:81], v[176:179], v[200:203], v[78:81]
	v_mfma_f32_16x16x32_bf16 v[70:73], v[168:171], v[208:211], v[70:73]
	v_mfma_f32_16x16x32_bf16 v[66:69], v[176:179], v[208:211], v[66:69]
	s_setprio 0
	s_barrier
	s_add_i32 s18, s18, s30
	v_lshl_add_u64 v[212:213], v[212:213], 0, s[12:13]
	s_mov_b32 m0, s18
	ds_read_b128 v[180:183], v150 offset:49152
	ds_read_b128 v[184:187], v150 offset:50176
	ds_read_b128 v[188:191], v150 offset:51200
	ds_read_b128 v[192:195], v150 offset:52224
	ds_read_b128 v[196:199], v150 offset:53248
	ds_read_b128 v[200:203], v150 offset:54272
	ds_read_b128 v[204:207], v150 offset:55296
	ds_read_b128 v[208:211], v150 offset:56320
	global_load_lds_dwordx4 v[212:213], off
	s_add_i32 m0, s18, 0x2000
	s_add_u32 s52, s52, 0x80080
	v_lshl_add_u64 v[212:213], v[214:215], 0, s[12:13]
	s_addc_u32 s53, s53, 0
	s_add_i32 s18, s19, s30
	global_load_lds_dwordx4 v[212:213], off
	v_lshl_add_u64 v[212:213], s[52:53], 0, v[132:133]
	s_mov_b32 m0, s18
	s_nop 0
	global_load_lds_dwordx4 v[212:213], off
	v_lshl_add_u64 v[212:213], s[52:53], 0, v[136:137]
	s_add_i32 m0, s18, 0x2000
	s_nop 0
	global_load_lds_dwordx4 v[212:213], off
	v_lshl_add_u64 v[212:213], v[216:217], 0, s[12:13]
	s_mov_b32 m0, s68
	s_nop 0
	global_load_lds_dwordx4 v[212:213], off
	v_lshl_add_u64 v[212:213], v[218:219], 0, s[12:13]
	s_mov_b32 m0, s69
	s_nop 0
	global_load_lds_dwordx4 v[212:213], off
	s_waitcnt vmcnt(8)
	s_waitcnt lgkmcnt(0)
	s_barrier
	s_setprio 1
	s_waitcnt lgkmcnt(0)
	v_mfma_f32_16x16x32_bf16 v[62:65], v[142:145], v[180:183], v[62:65]
	v_mfma_f32_16x16x32_bf16 v[58:61], v[156:159], v[180:183], v[58:61]
	v_mfma_f32_16x16x32_bf16 v[50:53], v[142:145], v[188:191], v[50:53]
	v_mfma_f32_16x16x32_bf16 v[42:45], v[156:159], v[188:191], v[42:45]
	v_mfma_f32_16x16x32_bf16 v[34:37], v[142:145], v[196:199], v[34:37]
	v_mfma_f32_16x16x32_bf16 v[26:29], v[156:159], v[196:199], v[26:29]
	v_mfma_f32_16x16x32_bf16 v[18:21], v[142:145], v[204:207], v[18:21]
	v_mfma_f32_16x16x32_bf16 v[10:13], v[156:159], v[204:207], v[10:13]
	v_mfma_f32_16x16x32_bf16 v[62:65], v[152:155], v[184:187], v[62:65]
	v_mfma_f32_16x16x32_bf16 v[58:61], v[160:163], v[184:187], v[58:61]
	v_mfma_f32_16x16x32_bf16 v[50:53], v[152:155], v[192:195], v[50:53]
	v_mfma_f32_16x16x32_bf16 v[42:45], v[160:163], v[192:195], v[42:45]
	v_mfma_f32_16x16x32_bf16 v[34:37], v[152:155], v[200:203], v[34:37]
	v_mfma_f32_16x16x32_bf16 v[26:29], v[160:163], v[200:203], v[26:29]
	v_mfma_f32_16x16x32_bf16 v[18:21], v[152:155], v[208:211], v[18:21]
	v_mfma_f32_16x16x32_bf16 v[10:13], v[160:163], v[208:211], v[10:13]
	s_setprio 0
	s_setprio 1
	v_mfma_f32_16x16x32_bf16 v[54:57], v[164:167], v[180:183], v[54:57]
	v_mfma_f32_16x16x32_bf16 v[46:49], v[172:175], v[180:183], v[46:49]
	v_mfma_f32_16x16x32_bf16 v[38:41], v[164:167], v[188:191], v[38:41]
	v_mfma_f32_16x16x32_bf16 v[30:33], v[172:175], v[188:191], v[30:33]
	v_mfma_f32_16x16x32_bf16 v[22:25], v[164:167], v[196:199], v[22:25]
	v_mfma_f32_16x16x32_bf16 v[14:17], v[172:175], v[196:199], v[14:17]
	v_mfma_f32_16x16x32_bf16 v[6:9], v[164:167], v[204:207], v[6:9]
	v_mfma_f32_16x16x32_bf16 v[2:5], v[172:175], v[204:207], v[2:5]
	v_mfma_f32_16x16x32_bf16 v[54:57], v[168:171], v[184:187], v[54:57]
	v_mfma_f32_16x16x32_bf16 v[46:49], v[176:179], v[184:187], v[46:49]
	v_mfma_f32_16x16x32_bf16 v[38:41], v[168:171], v[192:195], v[38:41]
	v_mfma_f32_16x16x32_bf16 v[30:33], v[176:179], v[192:195], v[30:33]
	v_mfma_f32_16x16x32_bf16 v[22:25], v[168:171], v[200:203], v[22:25]
	v_mfma_f32_16x16x32_bf16 v[14:17], v[176:179], v[200:203], v[14:17]
	v_mfma_f32_16x16x32_bf16 v[6:9], v[168:171], v[208:211], v[6:9]
	v_mfma_f32_16x16x32_bf16 v[2:5], v[176:179], v[208:211], v[2:5]
	s_add_i32 s87, s87, 2
	s_add_u32 s48, s48, 0x100
	s_addc_u32 s49, s49, 0
	s_add_u32 s58, s58, 0x100
	s_addc_u32 s59, s59, 0
	s_cmp_gt_u32 s87, 29
	s_barrier
	s_setprio 0
	s_cbranch_scc0 .LBB0_336
	s_and_b64 vcc, exec, s[14:15]
	s_cbranch_vccz .LBB0_339
	s_barrier

.LBB0_846:
	v_add_u32_e32 v2, s77, v162
	ds_read_b128 v[150:153], v2
	ds_read_b128 v[154:157], v2 offset:1024
	ds_read_b128 v[158:161], v2 offset:2048
	ds_read_b128 v[166:169], v2 offset:3072
	v_add_u32_e32 v2, s78, v162
	ds_read_b128 v[170:173], v2
	ds_read_b128 v[174:177], v2 offset:1024
	ds_read_b128 v[178:181], v2 offset:2048
	ds_read_b128 v[182:185], v2 offset:3072
	s_add_u32 s18, s54, 0xfff80080
	s_addc_u32 s19, s55, -1
	s_cmp_eq_u32 s87, 28
	s_cselect_b32 s63, s34, s19
	s_cselect_b32 s62, s35, s18
	s_cselect_b32 s59, s45, s86
	s_cselect_b32 s58, s47, s57
	v_lshl_add_u64 v[4:5], s[54:55], 0, v[142:143]
	s_add_i32 m0, s71, 0xc000
	ds_read_b128 v[186:189], v164
	ds_read_b128 v[190:193], v164 offset:1024
	ds_read_b128 v[194:197], v164 offset:2048
	ds_read_b128 v[198:201], v164 offset:3072
	ds_read_b128 v[202:205], v164 offset:4096
	ds_read_b128 v[206:209], v164 offset:5120
	ds_read_b128 v[210:213], v164 offset:6144
	ds_read_b128 v[214:217], v164 offset:7168
	global_load_lds_dwordx4 v[4:5], off
	v_lshl_add_u64 v[4:5], s[54:55], 0, v[144:145]
	s_add_i32 m0, s71, 0xe000
	s_nop 0
	global_load_lds_dwordx4 v[4:5], off
	s_waitcnt vmcnt(8)
	s_waitcnt lgkmcnt(0)
	s_barrier
	s_setprio 1
	s_waitcnt lgkmcnt(0)
	v_mfma_f32_16x16x32_bf16 v[130:133], v[150:153], v[186:189], v[130:133]
	v_mfma_f32_16x16x32_bf16 v[126:129], v[158:161], v[186:189], v[126:129]
	v_mfma_f32_16x16x32_bf16 v[122:125], v[150:153], v[194:197], v[122:125]
	v_mfma_f32_16x16x32_bf16 v[118:121], v[158:161], v[194:197], v[118:121]
	v_mfma_f32_16x16x32_bf16 v[114:117], v[150:153], v[202:205], v[114:117]
	v_mfma_f32_16x16x32_bf16 v[110:113], v[158:161], v[202:205], v[110:113]
	v_mfma_f32_16x16x32_bf16 v[106:109], v[150:153], v[210:213], v[106:109]
	v_mfma_f32_16x16x32_bf16 v[102:105], v[158:161], v[210:213], v[102:105]
	v_mfma_f32_16x16x32_bf16 v[130:133], v[154:157], v[190:193], v[130:133]
	v_mfma_f32_16x16x32_bf16 v[126:129], v[166:169], v[190:193], v[126:129]
	v_mfma_f32_16x16x32_bf16 v[122:125], v[154:157], v[198:201], v[122:125]
	v_mfma_f32_16x16x32_bf16 v[118:121], v[166:169], v[198:201], v[118:121]
	v_mfma_f32_16x16x32_bf16 v[114:117], v[154:157], v[206:209], v[114:117]
	v_mfma_f32_16x16x32_bf16 v[110:113], v[166:169], v[206:209], v[110:113]
	v_mfma_f32_16x16x32_bf16 v[106:109], v[154:157], v[214:217], v[106:109]
	v_mfma_f32_16x16x32_bf16 v[102:105], v[166:169], v[214:217], v[102:105]
	s_setprio 0
	s_setprio 1
	v_mfma_f32_16x16x32_bf16 v[98:101], v[170:173], v[186:189], v[98:101]
	v_mfma_f32_16x16x32_bf16 v[94:97], v[178:181], v[186:189], v[94:97]
	v_mfma_f32_16x16x32_bf16 v[90:93], v[170:173], v[194:197], v[90:93]
	v_mfma_f32_16x16x32_bf16 v[86:89], v[178:181], v[194:197], v[86:89]
	v_mfma_f32_16x16x32_bf16 v[82:85], v[170:173], v[202:205], v[82:85]
	v_mfma_f32_16x16x32_bf16 v[78:81], v[178:181], v[202:205], v[78:81]
	v_mfma_f32_16x16x32_bf16 v[74:77], v[170:173], v[210:213], v[74:77]
	v_mfma_f32_16x16x32_bf16 v[70:73], v[178:181], v[210:213], v[70:73]
	v_mfma_f32_16x16x32_bf16 v[98:101], v[174:177], v[190:193], v[98:101]
	v_mfma_f32_16x16x32_bf16 v[94:97], v[182:185], v[190:193], v[94:97]
	v_mfma_f32_16x16x32_bf16 v[90:93], v[174:177], v[198:201], v[90:93]
	v_mfma_f32_16x16x32_bf16 v[86:89], v[182:185], v[198:201], v[86:89]
	v_mfma_f32_16x16x32_bf16 v[82:85], v[174:177], v[206:209], v[82:85]
	v_mfma_f32_16x16x32_bf16 v[78:81], v[182:185], v[206:209], v[78:81]
	v_mfma_f32_16x16x32_bf16 v[74:77], v[174:177], v[214:217], v[74:77]
	v_mfma_f32_16x16x32_bf16 v[70:73], v[182:185], v[214:217], v[70:73]
	s_setprio 0
	s_barrier
	s_add_i32 s18, s77, s70
	v_lshl_add_u64 v[218:219], s[58:59], 0, v[136:137]
	s_mov_b32 m0, s18
	ds_read_b128 v[186:189], v164 offset:16384
	ds_read_b128 v[190:193], v164 offset:17408
	ds_read_b128 v[194:197], v164 offset:18432
	ds_read_b128 v[198:201], v164 offset:19456
	ds_read_b128 v[202:205], v164 offset:20480
	ds_read_b128 v[206:209], v164 offset:21504
	ds_read_b128 v[210:213], v164 offset:22528
	ds_read_b128 v[214:217], v164 offset:23552
	global_load_lds_dwordx4 v[218:219], off
	s_add_i32 m0, s18, 0x2000
	s_add_u32 s90, s58, 0x80000
	v_lshl_add_u64 v[220:221], s[58:59], 0, v[140:141]
	s_addc_u32 s91, s59, 0
	s_add_i32 s18, s78, s70
	global_load_lds_dwordx4 v[220:221], off
	v_lshl_add_u64 v[4:5], s[90:91], 0, v[136:137]
	s_mov_b32 m0, s18
	v_lshl_add_u64 v[222:223], s[62:63], 0, v[134:135]
	global_load_lds_dwordx4 v[4:5], off
	v_lshl_add_u64 v[4:5], s[90:91], 0, v[140:141]
	s_add_i32 m0, s18, 0x2000
	v_lshl_add_u64 v[224:225], s[62:63], 0, v[138:139]
	global_load_lds_dwordx4 v[4:5], off
	s_mov_b32 m0, s71
	s_nop 0
	global_load_lds_dwordx4 v[222:223], off
	s_mov_b32 m0, s72
	s_nop 0
	global_load_lds_dwordx4 v[224:225], off
	s_waitcnt vmcnt(8)
	s_waitcnt lgkmcnt(0)
	s_barrier
	s_setprio 1
	s_waitcnt lgkmcnt(0)
	v_mfma_f32_16x16x32_bf16 v[66:69], v[150:153], v[186:189], v[66:69]
	v_mfma_f32_16x16x32_bf16 v[62:65], v[158:161], v[186:189], v[62:65]
	v_mfma_f32_16x16x32_bf16 v[58:61], v[150:153], v[194:197], v[58:61]
	v_mfma_f32_16x16x32_bf16 v[54:57], v[158:161], v[194:197], v[54:57]
	v_mfma_f32_16x16x32_bf16 v[50:53], v[150:153], v[202:205], v[50:53]
	v_mfma_f32_16x16x32_bf16 v[46:49], v[158:161], v[202:205], v[46:49]
	v_mfma_f32_16x16x32_bf16 v[42:45], v[150:153], v[210:213], v[42:45]
	v_mfma_f32_16x16x32_bf16 v[38:41], v[158:161], v[210:213], v[38:41]
	v_mfma_f32_16x16x32_bf16 v[66:69], v[154:157], v[190:193], v[66:69]
	v_mfma_f32_16x16x32_bf16 v[62:65], v[166:169], v[190:193], v[62:65]
	v_mfma_f32_16x16x32_bf16 v[58:61], v[154:157], v[198:201], v[58:61]
	v_mfma_f32_16x16x32_bf16 v[54:57], v[166:169], v[198:201], v[54:57]
	v_mfma_f32_16x16x32_bf16 v[50:53], v[154:157], v[206:209], v[50:53]
	v_mfma_f32_16x16x32_bf16 v[46:49], v[166:169], v[206:209], v[46:49]
	v_mfma_f32_16x16x32_bf16 v[42:45], v[154:157], v[214:217], v[42:45]
	v_mfma_f32_16x16x32_bf16 v[38:41], v[166:169], v[214:217], v[38:41]
	s_setprio 0
	s_setprio 1
	v_mfma_f32_16x16x32_bf16 v[34:37], v[170:173], v[186:189], v[34:37]
	v_mfma_f32_16x16x32_bf16 v[30:33], v[178:181], v[186:189], v[30:33]
	v_mfma_f32_16x16x32_bf16 v[26:29], v[170:173], v[194:197], v[26:29]
	v_mfma_f32_16x16x32_bf16 v[22:25], v[178:181], v[194:197], v[22:25]
	v_mfma_f32_16x16x32_bf16 v[18:21], v[170:173], v[202:205], v[18:21]
	v_mfma_f32_16x16x32_bf16 v[14:17], v[178:181], v[202:205], v[14:17]
	v_mfma_f32_16x16x32_bf16 v[10:13], v[170:173], v[210:213], v[10:13]
	v_mfma_f32_16x16x32_bf16 v[4:7], v[178:181], v[210:213], v[6:9]
	v_mfma_f32_16x16x32_bf16 v[34:37], v[174:177], v[190:193], v[34:37]
	v_mfma_f32_16x16x32_bf16 v[30:33], v[182:185], v[190:193], v[30:33]
	v_mfma_f32_16x16x32_bf16 v[26:29], v[174:177], v[198:201], v[26:29]
	v_mfma_f32_16x16x32_bf16 v[22:25], v[182:185], v[198:201], v[22:25]
	v_mfma_f32_16x16x32_bf16 v[18:21], v[174:177], v[206:209], v[18:21]
	v_mfma_f32_16x16x32_bf16 v[14:17], v[182:185], v[206:209], v[14:17]
	v_mfma_f32_16x16x32_bf16 v[10:13], v[174:177], v[214:217], v[10:13]
	v_mfma_f32_16x16x32_bf16 v[4:7], v[182:185], v[214:217], v[4:7]
	s_setprio 0
	s_barrier
	s_add_i32 s18, 0, 0x18000
	v_add_u32_e32 v2, s18, v162
	s_add_i32 s19, 0, 0x1c000
	ds_read_b128 v[150:153], v2
	ds_read_b128 v[154:157], v2 offset:1024
	ds_read_b128 v[158:161], v2 offset:2048
	ds_read_b128 v[166:169], v2 offset:3072
	v_add_u32_e32 v2, s19, v162
	ds_read_b128 v[170:173], v2
	ds_read_b128 v[174:177], v2 offset:1024
	ds_read_b128 v[178:181], v2 offset:2048
	ds_read_b128 v[182:185], v2 offset:3072
	s_add_u32 s62, s62, 0x80000
	s_addc_u32 s63, s63, 0
	s_mov_b32 m0, s73
	v_lshl_add_u64 v[8:9], s[62:63], 0, v[134:135]
	ds_read_b128 v[186:189], v164 offset:32768
	ds_read_b128 v[190:193], v164 offset:33792
	ds_read_b128 v[194:197], v164 offset:34816
	ds_read_b128 v[198:201], v164 offset:35840
	ds_read_b128 v[202:205], v164 offset:36864
	ds_read_b128 v[206:209], v164 offset:37888
	ds_read_b128 v[210:213], v164 offset:38912
	ds_read_b128 v[214:217], v164 offset:39936
	global_load_lds_dwordx4 v[8:9], off
	v_lshl_add_u64 v[8:9], s[62:63], 0, v[138:139]
	s_mov_b32 m0, s74
	s_nop 0
	global_load_lds_dwordx4 v[8:9], off
	s_waitcnt vmcnt(8)
	s_waitcnt lgkmcnt(0)
	s_barrier
	s_setprio 1
	s_waitcnt lgkmcnt(0)
	v_mfma_f32_16x16x32_bf16 v[130:133], v[150:153], v[186:189], v[130:133]
	v_mfma_f32_16x16x32_bf16 v[126:129], v[158:161], v[186:189], v[126:129]
	v_mfma_f32_16x16x32_bf16 v[122:125], v[150:153], v[194:197], v[122:125]
	v_mfma_f32_16x16x32_bf16 v[118:121], v[158:161], v[194:197], v[118:121]
	v_mfma_f32_16x16x32_bf16 v[114:117], v[150:153], v[202:205], v[114:117]
	v_mfma_f32_16x16x32_bf16 v[110:113], v[158:161], v[202:205], v[110:113]
	v_mfma_f32_16x16x32_bf16 v[106:109], v[150:153], v[210:213], v[106:109]
	v_mfma_f32_16x16x32_bf16 v[102:105], v[158:161], v[210:213], v[102:105]
	v_mfma_f32_16x16x32_bf16 v[130:133], v[154:157], v[190:193], v[130:133]
	v_mfma_f32_16x16x32_bf16 v[126:129], v[166:169], v[190:193], v[126:129]
	v_mfma_f32_16x16x32_bf16 v[122:125], v[154:157], v[198:201], v[122:125]
	v_mfma_f32_16x16x32_bf16 v[118:121], v[166:169], v[198:201], v[118:121]
	v_mfma_f32_16x16x32_bf16 v[114:117], v[154:157], v[206:209], v[114:117]
	v_mfma_f32_16x16x32_bf16 v[110:113], v[166:169], v[206:209], v[110:113]
	v_mfma_f32_16x16x32_bf16 v[106:109], v[154:157], v[214:217], v[106:109]
	v_mfma_f32_16x16x32_bf16 v[102:105], v[166:169], v[214:217], v[102:105]
	s_setprio 0
	s_setprio 1
	v_mfma_f32_16x16x32_bf16 v[98:101], v[170:173], v[186:189], v[98:101]
	v_mfma_f32_16x16x32_bf16 v[94:97], v[178:181], v[186:189], v[94:97]
	v_mfma_f32_16x16x32_bf16 v[90:93], v[170:173], v[194:197], v[90:93]
	v_mfma_f32_16x16x32_bf16 v[86:89], v[178:181], v[194:197], v[86:89]
	v_mfma_f32_16x16x32_bf16 v[82:85], v[170:173], v[202:205], v[82:85]
	v_mfma_f32_16x16x32_bf16 v[78:81], v[178:181], v[202:205], v[78:81]
	v_mfma_f32_16x16x32_bf16 v[74:77], v[170:173], v[210:213], v[74:77]
	v_mfma_f32_16x16x32_bf16 v[70:73], v[178:181], v[210:213], v[70:73]
	v_mfma_f32_16x16x32_bf16 v[98:101], v[174:177], v[190:193], v[98:101]
	v_mfma_f32_16x16x32_bf16 v[94:97], v[182:185], v[190:193], v[94:97]
	v_mfma_f32_16x16x32_bf16 v[90:93], v[174:177], v[198:201], v[90:93]
	v_mfma_f32_16x16x32_bf16 v[86:89], v[182:185], v[198:201], v[86:89]
	v_mfma_f32_16x16x32_bf16 v[82:85], v[174:177], v[206:209], v[82:85]
	v_mfma_f32_16x16x32_bf16 v[78:81], v[182:185], v[206:209], v[78:81]
	v_mfma_f32_16x16x32_bf16 v[74:77], v[174:177], v[214:217], v[74:77]
	v_mfma_f32_16x16x32_bf16 v[70:73], v[182:185], v[214:217], v[70:73]
	s_setprio 0
	s_barrier
	s_add_i32 s18, s18, s70
	v_lshl_add_u64 v[8:9], v[218:219], 0, s[14:15]
	s_mov_b32 m0, s18
	ds_read_b128 v[186:189], v164 offset:49152
	ds_read_b128 v[190:193], v164 offset:50176
	ds_read_b128 v[194:197], v164 offset:51200
	ds_read_b128 v[198:201], v164 offset:52224
	ds_read_b128 v[202:205], v164 offset:53248
	ds_read_b128 v[206:209], v164 offset:54272
	ds_read_b128 v[210:213], v164 offset:55296
	ds_read_b128 v[214:217], v164 offset:56320
	global_load_lds_dwordx4 v[8:9], off
	s_add_i32 m0, s18, 0x2000
	s_add_u32 s58, s58, 0x80080
	v_lshl_add_u64 v[8:9], v[220:221], 0, s[14:15]
	s_addc_u32 s59, s59, 0
	s_add_i32 s18, s19, s70
	global_load_lds_dwordx4 v[8:9], off
	v_lshl_add_u64 v[8:9], s[58:59], 0, v[136:137]
	s_mov_b32 m0, s18
	s_nop 0
	global_load_lds_dwordx4 v[8:9], off
	v_lshl_add_u64 v[8:9], s[58:59], 0, v[140:141]
	s_add_i32 m0, s18, 0x2000
	s_nop 0
	global_load_lds_dwordx4 v[8:9], off
	v_lshl_add_u64 v[8:9], v[222:223], 0, s[14:15]
	s_mov_b32 m0, s75
	s_nop 0
	global_load_lds_dwordx4 v[8:9], off
	v_lshl_add_u64 v[8:9], v[224:225], 0, s[14:15]
	s_mov_b32 m0, s76
	s_nop 0
	global_load_lds_dwordx4 v[8:9], off
	s_waitcnt vmcnt(8)
	s_waitcnt lgkmcnt(0)
	s_barrier
	s_setprio 1
	s_waitcnt lgkmcnt(0)
	v_mfma_f32_16x16x32_bf16 v[66:69], v[150:153], v[186:189], v[66:69]
	v_mfma_f32_16x16x32_bf16 v[62:65], v[158:161], v[186:189], v[62:65]
	v_mfma_f32_16x16x32_bf16 v[58:61], v[150:153], v[194:197], v[58:61]
	v_mfma_f32_16x16x32_bf16 v[54:57], v[158:161], v[194:197], v[54:57]
	v_mfma_f32_16x16x32_bf16 v[50:53], v[150:153], v[202:205], v[50:53]
	v_mfma_f32_16x16x32_bf16 v[46:49], v[158:161], v[202:205], v[46:49]
	v_mfma_f32_16x16x32_bf16 v[42:45], v[150:153], v[210:213], v[42:45]
	v_mfma_f32_16x16x32_bf16 v[38:41], v[158:161], v[210:213], v[38:41]
	v_mfma_f32_16x16x32_bf16 v[66:69], v[154:157], v[190:193], v[66:69]
	v_mfma_f32_16x16x32_bf16 v[62:65], v[166:169], v[190:193], v[62:65]
	v_mfma_f32_16x16x32_bf16 v[58:61], v[154:157], v[198:201], v[58:61]
	v_mfma_f32_16x16x32_bf16 v[54:57], v[166:169], v[198:201], v[54:57]
	v_mfma_f32_16x16x32_bf16 v[50:53], v[154:157], v[206:209], v[50:53]
	v_mfma_f32_16x16x32_bf16 v[46:49], v[166:169], v[206:209], v[46:49]
	v_mfma_f32_16x16x32_bf16 v[42:45], v[154:157], v[214:217], v[42:45]
	v_mfma_f32_16x16x32_bf16 v[38:41], v[166:169], v[214:217], v[38:41]
	s_setprio 0
	s_setprio 1
	v_mfma_f32_16x16x32_bf16 v[34:37], v[170:173], v[186:189], v[34:37]
	v_mfma_f32_16x16x32_bf16 v[30:33], v[178:181], v[186:189], v[30:33]
	v_mfma_f32_16x16x32_bf16 v[26:29], v[170:173], v[194:197], v[26:29]
	v_mfma_f32_16x16x32_bf16 v[22:25], v[178:181], v[194:197], v[22:25]
	v_mfma_f32_16x16x32_bf16 v[18:21], v[170:173], v[202:205], v[18:21]
	v_mfma_f32_16x16x32_bf16 v[14:17], v[178:181], v[202:205], v[14:17]
	v_mfma_f32_16x16x32_bf16 v[8:11], v[170:173], v[210:213], v[10:13]
	v_mfma_f32_16x16x32_bf16 v[4:7], v[178:181], v[210:213], v[4:7]
	v_mfma_f32_16x16x32_bf16 v[34:37], v[174:177], v[190:193], v[34:37]
	v_mfma_f32_16x16x32_bf16 v[30:33], v[182:185], v[190:193], v[30:33]
	v_mfma_f32_16x16x32_bf16 v[26:29], v[174:177], v[198:201], v[26:29]
	v_mfma_f32_16x16x32_bf16 v[22:25], v[182:185], v[198:201], v[22:25]
	v_mfma_f32_16x16x32_bf16 v[18:21], v[174:177], v[206:209], v[18:21]
	v_mfma_f32_16x16x32_bf16 v[14:17], v[182:185], v[206:209], v[14:17]
	v_mfma_f32_16x16x32_bf16 v[10:13], v[174:177], v[214:217], v[8:11]
	v_mfma_f32_16x16x32_bf16 v[6:9], v[182:185], v[214:217], v[4:7]
	s_add_i32 s87, s87, 2
	s_add_u32 s54, s54, 0x100
	s_addc_u32 s55, s55, 0
	s_add_u32 s57, s57, 0x100
	s_addc_u32 s86, s86, 0
	s_cmp_gt_u32 s87, 29
	s_barrier
	s_setprio 0
	s_cbranch_scc0 .LBB0_846
	s_and_b64 vcc, exec, s[16:17]
	s_cbranch_vccz .LBB0_849
	s_barrier

.LBB0_927:
	ds_read_b128 v[130:133], v166
	ds_read_b128 v[134:137], v166 offset:1024
	ds_read_b128 v[138:141], v166 offset:2048
	ds_read_b128 v[142:145], v166 offset:3072
	ds_read_b128 v[170:173], v167
	ds_read_b128 v[174:177], v167 offset:1024
	ds_read_b128 v[178:181], v167 offset:2048
	ds_read_b128 v[182:185], v167 offset:3072
	s_add_u32 s18, s56, 0xfff80080
	s_addc_u32 s19, s57, -1
	s_cmp_eq_u32 s86, 28
	s_cselect_b32 s63, s47, s19
	s_cselect_b32 s62, s82, s18
	s_cselect_b32 s59, s45, s85
	s_cselect_b32 s58, s83, s84
	v_lshl_add_u64 v[162:163], s[56:57], 0, v[154:155]
	s_add_i32 m0, s55, 0xc000
	ds_read_b128 v[186:189], v168
	ds_read_b128 v[190:193], v168 offset:1024
	ds_read_b128 v[194:197], v168 offset:2048
	ds_read_b128 v[198:201], v168 offset:3072
	ds_read_b128 v[202:205], v168 offset:4096
	ds_read_b128 v[206:209], v168 offset:5120
	ds_read_b128 v[210:213], v168 offset:6144
	ds_read_b128 v[214:217], v168 offset:7168
	global_load_lds_dwordx4 v[162:163], off
	v_lshl_add_u64 v[162:163], s[56:57], 0, v[156:157]
	s_add_i32 m0, s55, 0xe000
	s_nop 0
	global_load_lds_dwordx4 v[162:163], off
	s_waitcnt vmcnt(8)
	s_waitcnt lgkmcnt(0)
	s_barrier
	s_setprio 1
	s_waitcnt lgkmcnt(0)
	v_mfma_f32_16x16x32_bf16 v[122:125], v[130:133], v[186:189], v[122:125]
	v_mfma_f32_16x16x32_bf16 v[126:129], v[138:141], v[186:189], v[126:129]
	v_mfma_f32_16x16x32_bf16 v[114:117], v[130:133], v[194:197], v[114:117]
	v_mfma_f32_16x16x32_bf16 v[118:121], v[138:141], v[194:197], v[118:121]
	v_mfma_f32_16x16x32_bf16 v[102:105], v[130:133], v[202:205], v[102:105]
	v_mfma_f32_16x16x32_bf16 v[110:113], v[138:141], v[202:205], v[110:113]
	v_mfma_f32_16x16x32_bf16 v[94:97], v[130:133], v[210:213], v[94:97]
	v_mfma_f32_16x16x32_bf16 v[74:77], v[138:141], v[210:213], v[74:77]
	v_mfma_f32_16x16x32_bf16 v[122:125], v[134:137], v[190:193], v[122:125]
	v_mfma_f32_16x16x32_bf16 v[126:129], v[142:145], v[190:193], v[126:129]
	v_mfma_f32_16x16x32_bf16 v[114:117], v[134:137], v[198:201], v[114:117]
	v_mfma_f32_16x16x32_bf16 v[118:121], v[142:145], v[198:201], v[118:121]
	v_mfma_f32_16x16x32_bf16 v[102:105], v[134:137], v[206:209], v[102:105]
	v_mfma_f32_16x16x32_bf16 v[110:113], v[142:145], v[206:209], v[110:113]
	v_mfma_f32_16x16x32_bf16 v[94:97], v[134:137], v[214:217], v[94:97]
	v_mfma_f32_16x16x32_bf16 v[74:77], v[142:145], v[214:217], v[74:77]
	s_setprio 0
	s_setprio 1
	v_mfma_f32_16x16x32_bf16 v[106:109], v[170:173], v[186:189], v[106:109]
	v_mfma_f32_16x16x32_bf16 v[90:93], v[178:181], v[186:189], v[90:93]
	v_mfma_f32_16x16x32_bf16 v[98:101], v[170:173], v[194:197], v[98:101]
	v_mfma_f32_16x16x32_bf16 v[82:85], v[178:181], v[194:197], v[82:85]
	v_mfma_f32_16x16x32_bf16 v[86:89], v[170:173], v[202:205], v[86:89]
	v_mfma_f32_16x16x32_bf16 v[78:81], v[178:181], v[202:205], v[78:81]
	v_mfma_f32_16x16x32_bf16 v[70:73], v[170:173], v[210:213], v[70:73]
	v_mfma_f32_16x16x32_bf16 v[66:69], v[178:181], v[210:213], v[66:69]
	v_mfma_f32_16x16x32_bf16 v[106:109], v[174:177], v[190:193], v[106:109]
	v_mfma_f32_16x16x32_bf16 v[90:93], v[182:185], v[190:193], v[90:93]
	v_mfma_f32_16x16x32_bf16 v[98:101], v[174:177], v[198:201], v[98:101]
	v_mfma_f32_16x16x32_bf16 v[82:85], v[182:185], v[198:201], v[82:85]
	v_mfma_f32_16x16x32_bf16 v[86:89], v[174:177], v[206:209], v[86:89]
	v_mfma_f32_16x16x32_bf16 v[78:81], v[182:185], v[206:209], v[78:81]
	v_mfma_f32_16x16x32_bf16 v[70:73], v[174:177], v[214:217], v[70:73]
	v_mfma_f32_16x16x32_bf16 v[66:69], v[182:185], v[214:217], v[66:69]
	s_setprio 0
	s_barrier
	s_add_i32 s18, s74, s66
	v_lshl_add_u64 v[162:163], s[58:59], 0, v[148:149]
	s_mov_b32 m0, s18
	ds_read_b128 v[186:189], v168 offset:16384
	ds_read_b128 v[190:193], v168 offset:17408
	ds_read_b128 v[194:197], v168 offset:18432
	ds_read_b128 v[198:201], v168 offset:19456
	ds_read_b128 v[202:205], v168 offset:20480
	ds_read_b128 v[206:209], v168 offset:21504
	ds_read_b128 v[210:213], v168 offset:22528
	ds_read_b128 v[214:217], v168 offset:23552
	global_load_lds_dwordx4 v[162:163], off
	s_add_i32 m0, s18, 0x2000
	s_add_u32 s90, s58, 0x80000
	v_lshl_add_u64 v[218:219], s[58:59], 0, v[152:153]
	s_addc_u32 s91, s59, 0
	s_add_i32 s18, s75, s66
	global_load_lds_dwordx4 v[218:219], off
	v_lshl_add_u64 v[220:221], s[90:91], 0, v[148:149]
	s_mov_b32 m0, s18
	v_lshl_add_u64 v[222:223], s[62:63], 0, v[150:151]
	global_load_lds_dwordx4 v[220:221], off
	v_lshl_add_u64 v[220:221], s[90:91], 0, v[152:153]
	s_add_i32 m0, s18, 0x2000
	s_nop 0
	global_load_lds_dwordx4 v[220:221], off
	v_lshl_add_u64 v[220:221], s[62:63], 0, v[146:147]
	s_mov_b32 m0, s55
	s_nop 0
	global_load_lds_dwordx4 v[220:221], off
	s_mov_b32 m0, s67
	s_nop 0
	global_load_lds_dwordx4 v[222:223], off
	s_waitcnt vmcnt(8)
	s_waitcnt lgkmcnt(0)
	s_barrier
	s_setprio 1
	s_waitcnt lgkmcnt(0)
	v_mfma_f32_16x16x32_bf16 v[62:65], v[130:133], v[186:189], v[62:65]
	v_mfma_f32_16x16x32_bf16 v[58:61], v[138:141], v[186:189], v[58:61]
	v_mfma_f32_16x16x32_bf16 v[50:53], v[130:133], v[194:197], v[50:53]
	v_mfma_f32_16x16x32_bf16 v[42:45], v[138:141], v[194:197], v[42:45]
	v_mfma_f32_16x16x32_bf16 v[34:37], v[130:133], v[202:205], v[34:37]
	v_mfma_f32_16x16x32_bf16 v[26:29], v[138:141], v[202:205], v[26:29]
	v_mfma_f32_16x16x32_bf16 v[18:21], v[130:133], v[210:213], v[18:21]
	v_mfma_f32_16x16x32_bf16 v[10:13], v[138:141], v[210:213], v[10:13]
	v_mfma_f32_16x16x32_bf16 v[62:65], v[134:137], v[190:193], v[62:65]
	v_mfma_f32_16x16x32_bf16 v[58:61], v[142:145], v[190:193], v[58:61]
	v_mfma_f32_16x16x32_bf16 v[50:53], v[134:137], v[198:201], v[50:53]
	v_mfma_f32_16x16x32_bf16 v[42:45], v[142:145], v[198:201], v[42:45]
	v_mfma_f32_16x16x32_bf16 v[34:37], v[134:137], v[206:209], v[34:37]
	v_mfma_f32_16x16x32_bf16 v[26:29], v[142:145], v[206:209], v[26:29]
	v_mfma_f32_16x16x32_bf16 v[18:21], v[134:137], v[214:217], v[18:21]
	v_mfma_f32_16x16x32_bf16 v[10:13], v[142:145], v[214:217], v[10:13]
	s_setprio 0
	s_setprio 1
	v_mfma_f32_16x16x32_bf16 v[54:57], v[170:173], v[186:189], v[54:57]
	v_mfma_f32_16x16x32_bf16 v[46:49], v[178:181], v[186:189], v[46:49]
	v_mfma_f32_16x16x32_bf16 v[38:41], v[170:173], v[194:197], v[38:41]
	v_mfma_f32_16x16x32_bf16 v[30:33], v[178:181], v[194:197], v[30:33]
	v_mfma_f32_16x16x32_bf16 v[22:25], v[170:173], v[202:205], v[22:25]
	v_mfma_f32_16x16x32_bf16 v[14:17], v[178:181], v[202:205], v[14:17]
	v_mfma_f32_16x16x32_bf16 v[6:9], v[170:173], v[210:213], v[6:9]
	v_mfma_f32_16x16x32_bf16 v[2:5], v[178:181], v[210:213], v[2:5]
	v_mfma_f32_16x16x32_bf16 v[54:57], v[174:177], v[190:193], v[54:57]
	v_mfma_f32_16x16x32_bf16 v[46:49], v[182:185], v[190:193], v[46:49]
	v_mfma_f32_16x16x32_bf16 v[38:41], v[174:177], v[198:201], v[38:41]
	v_mfma_f32_16x16x32_bf16 v[30:33], v[182:185], v[198:201], v[30:33]
	v_mfma_f32_16x16x32_bf16 v[22:25], v[174:177], v[206:209], v[22:25]
	v_mfma_f32_16x16x32_bf16 v[14:17], v[182:185], v[206:209], v[14:17]
	v_mfma_f32_16x16x32_bf16 v[6:9], v[174:177], v[214:217], v[6:9]
	v_mfma_f32_16x16x32_bf16 v[2:5], v[182:185], v[214:217], v[2:5]
	s_setprio 0
	s_barrier
	s_add_i32 s18, 0, 0x18000
	s_add_i32 s19, 0, 0x1c000
	v_add_u32_e32 v142, s18, v164
	v_add_u32_e32 v169, s19, v164
	ds_read_b128 v[130:133], v142
	ds_read_b128 v[134:137], v142 offset:1024
	ds_read_b128 v[138:141], v142 offset:2048
	ds_read_b128 v[142:145], v142 offset:3072
	ds_read_b128 v[170:173], v169
	ds_read_b128 v[174:177], v169 offset:1024
	ds_read_b128 v[178:181], v169 offset:2048
	ds_read_b128 v[182:185], v169 offset:3072
	s_add_u32 s62, s62, 0x80000
	s_addc_u32 s63, s63, 0
	s_mov_b32 m0, s68
	v_lshl_add_u64 v[224:225], s[62:63], 0, v[146:147]
	ds_read_b128 v[186:189], v168 offset:32768
	ds_read_b128 v[190:193], v168 offset:33792
	ds_read_b128 v[194:197], v168 offset:34816
	ds_read_b128 v[198:201], v168 offset:35840
	ds_read_b128 v[202:205], v168 offset:36864
	ds_read_b128 v[206:209], v168 offset:37888
	ds_read_b128 v[210:213], v168 offset:38912
	ds_read_b128 v[214:217], v168 offset:39936
	global_load_lds_dwordx4 v[224:225], off
	v_lshl_add_u64 v[224:225], s[62:63], 0, v[150:151]
	s_mov_b32 m0, s69
	s_nop 0
	global_load_lds_dwordx4 v[224:225], off
	s_waitcnt vmcnt(8)
	s_waitcnt lgkmcnt(0)
	s_barrier
	s_setprio 1
	s_waitcnt lgkmcnt(0)
	v_mfma_f32_16x16x32_bf16 v[122:125], v[130:133], v[186:189], v[122:125]
	v_mfma_f32_16x16x32_bf16 v[126:129], v[138:141], v[186:189], v[126:129]
	v_mfma_f32_16x16x32_bf16 v[114:117], v[130:133], v[194:197], v[114:117]
	v_mfma_f32_16x16x32_bf16 v[118:121], v[138:141], v[194:197], v[118:121]
	v_mfma_f32_16x16x32_bf16 v[102:105], v[130:133], v[202:205], v[102:105]
	v_mfma_f32_16x16x32_bf16 v[110:113], v[138:141], v[202:205], v[110:113]
	v_mfma_f32_16x16x32_bf16 v[94:97], v[130:133], v[210:213], v[94:97]
	v_mfma_f32_16x16x32_bf16 v[74:77], v[138:141], v[210:213], v[74:77]
	v_mfma_f32_16x16x32_bf16 v[122:125], v[134:137], v[190:193], v[122:125]
	v_mfma_f32_16x16x32_bf16 v[126:129], v[142:145], v[190:193], v[126:129]
	v_mfma_f32_16x16x32_bf16 v[114:117], v[134:137], v[198:201], v[114:117]
	v_mfma_f32_16x16x32_bf16 v[118:121], v[142:145], v[198:201], v[118:121]
	v_mfma_f32_16x16x32_bf16 v[102:105], v[134:137], v[206:209], v[102:105]
	v_mfma_f32_16x16x32_bf16 v[110:113], v[142:145], v[206:209], v[110:113]
	v_mfma_f32_16x16x32_bf16 v[94:97], v[134:137], v[214:217], v[94:97]
	v_mfma_f32_16x16x32_bf16 v[74:77], v[142:145], v[214:217], v[74:77]
	s_setprio 0
	s_setprio 1
	v_mfma_f32_16x16x32_bf16 v[106:109], v[170:173], v[186:189], v[106:109]
	v_mfma_f32_16x16x32_bf16 v[90:93], v[178:181], v[186:189], v[90:93]
	v_mfma_f32_16x16x32_bf16 v[98:101], v[170:173], v[194:197], v[98:101]
	v_mfma_f32_16x16x32_bf16 v[82:85], v[178:181], v[194:197], v[82:85]
	v_mfma_f32_16x16x32_bf16 v[86:89], v[170:173], v[202:205], v[86:89]
	v_mfma_f32_16x16x32_bf16 v[78:81], v[178:181], v[202:205], v[78:81]
	v_mfma_f32_16x16x32_bf16 v[70:73], v[170:173], v[210:213], v[70:73]
	v_mfma_f32_16x16x32_bf16 v[66:69], v[178:181], v[210:213], v[66:69]
	v_mfma_f32_16x16x32_bf16 v[106:109], v[174:177], v[190:193], v[106:109]
	v_mfma_f32_16x16x32_bf16 v[90:93], v[182:185], v[190:193], v[90:93]
	v_mfma_f32_16x16x32_bf16 v[98:101], v[174:177], v[198:201], v[98:101]
	v_mfma_f32_16x16x32_bf16 v[82:85], v[182:185], v[198:201], v[82:85]
	v_mfma_f32_16x16x32_bf16 v[86:89], v[174:177], v[206:209], v[86:89]
	v_mfma_f32_16x16x32_bf16 v[78:81], v[182:185], v[206:209], v[78:81]
	v_mfma_f32_16x16x32_bf16 v[70:73], v[174:177], v[214:217], v[70:73]
	v_mfma_f32_16x16x32_bf16 v[66:69], v[182:185], v[214:217], v[66:69]
	s_setprio 0
	s_barrier
	s_add_i32 s18, s18, s66
	v_lshl_add_u64 v[162:163], v[162:163], 0, s[12:13]
	s_mov_b32 m0, s18
	ds_read_b128 v[186:189], v168 offset:49152
	ds_read_b128 v[190:193], v168 offset:50176
	ds_read_b128 v[194:197], v168 offset:51200
	ds_read_b128 v[198:201], v168 offset:52224
	ds_read_b128 v[202:205], v168 offset:53248
	ds_read_b128 v[206:209], v168 offset:54272
	ds_read_b128 v[210:213], v168 offset:55296
	ds_read_b128 v[214:217], v168 offset:56320
	global_load_lds_dwordx4 v[162:163], off
	s_add_i32 m0, s18, 0x2000
	s_add_u32 s58, s58, 0x80080
	v_lshl_add_u64 v[162:163], v[218:219], 0, s[12:13]
	s_addc_u32 s59, s59, 0
	s_add_i32 s18, s19, s66
	global_load_lds_dwordx4 v[162:163], off
	v_lshl_add_u64 v[162:163], s[58:59], 0, v[148:149]
	s_mov_b32 m0, s18
	s_nop 0
	global_load_lds_dwordx4 v[162:163], off
	v_lshl_add_u64 v[162:163], s[58:59], 0, v[152:153]
	s_add_i32 m0, s18, 0x2000
	s_nop 0
	global_load_lds_dwordx4 v[162:163], off
	v_lshl_add_u64 v[162:163], v[220:221], 0, s[12:13]
	s_mov_b32 m0, s72
	s_nop 0
	global_load_lds_dwordx4 v[162:163], off
	v_lshl_add_u64 v[162:163], v[222:223], 0, s[12:13]
	s_mov_b32 m0, s73
	s_nop 0
	global_load_lds_dwordx4 v[162:163], off
	s_waitcnt vmcnt(8)
	s_waitcnt lgkmcnt(0)
	s_barrier
	s_setprio 1
	s_waitcnt lgkmcnt(0)
	v_mfma_f32_16x16x32_bf16 v[62:65], v[130:133], v[186:189], v[62:65]
	v_mfma_f32_16x16x32_bf16 v[58:61], v[138:141], v[186:189], v[58:61]
	v_mfma_f32_16x16x32_bf16 v[50:53], v[130:133], v[194:197], v[50:53]
	v_mfma_f32_16x16x32_bf16 v[42:45], v[138:141], v[194:197], v[42:45]
	v_mfma_f32_16x16x32_bf16 v[34:37], v[130:133], v[202:205], v[34:37]
	v_mfma_f32_16x16x32_bf16 v[26:29], v[138:141], v[202:205], v[26:29]
	v_mfma_f32_16x16x32_bf16 v[18:21], v[130:133], v[210:213], v[18:21]
	v_mfma_f32_16x16x32_bf16 v[10:13], v[138:141], v[210:213], v[10:13]
	v_mfma_f32_16x16x32_bf16 v[62:65], v[134:137], v[190:193], v[62:65]
	v_mfma_f32_16x16x32_bf16 v[58:61], v[142:145], v[190:193], v[58:61]
	v_mfma_f32_16x16x32_bf16 v[50:53], v[134:137], v[198:201], v[50:53]
	v_mfma_f32_16x16x32_bf16 v[42:45], v[142:145], v[198:201], v[42:45]
	v_mfma_f32_16x16x32_bf16 v[34:37], v[134:137], v[206:209], v[34:37]
	v_mfma_f32_16x16x32_bf16 v[26:29], v[142:145], v[206:209], v[26:29]
	v_mfma_f32_16x16x32_bf16 v[18:21], v[134:137], v[214:217], v[18:21]
	v_mfma_f32_16x16x32_bf16 v[10:13], v[142:145], v[214:217], v[10:13]
	s_setprio 0
	s_setprio 1
	v_mfma_f32_16x16x32_bf16 v[54:57], v[170:173], v[186:189], v[54:57]
	v_mfma_f32_16x16x32_bf16 v[46:49], v[178:181], v[186:189], v[46:49]
	v_mfma_f32_16x16x32_bf16 v[38:41], v[170:173], v[194:197], v[38:41]
	v_mfma_f32_16x16x32_bf16 v[30:33], v[178:181], v[194:197], v[30:33]
	v_mfma_f32_16x16x32_bf16 v[22:25], v[170:173], v[202:205], v[22:25]
	v_mfma_f32_16x16x32_bf16 v[14:17], v[178:181], v[202:205], v[14:17]
	v_mfma_f32_16x16x32_bf16 v[6:9], v[170:173], v[210:213], v[6:9]
	v_mfma_f32_16x16x32_bf16 v[2:5], v[178:181], v[210:213], v[2:5]
	v_mfma_f32_16x16x32_bf16 v[54:57], v[174:177], v[190:193], v[54:57]
	v_mfma_f32_16x16x32_bf16 v[46:49], v[182:185], v[190:193], v[46:49]
	v_mfma_f32_16x16x32_bf16 v[38:41], v[174:177], v[198:201], v[38:41]
	v_mfma_f32_16x16x32_bf16 v[30:33], v[182:185], v[198:201], v[30:33]
	v_mfma_f32_16x16x32_bf16 v[22:25], v[174:177], v[206:209], v[22:25]
	v_mfma_f32_16x16x32_bf16 v[14:17], v[182:185], v[206:209], v[14:17]
	v_mfma_f32_16x16x32_bf16 v[6:9], v[174:177], v[214:217], v[6:9]
	v_mfma_f32_16x16x32_bf16 v[2:5], v[182:185], v[214:217], v[2:5]
	s_add_i32 s86, s86, 2
	s_add_u32 s56, s56, 0x100
	s_addc_u32 s57, s57, 0
	s_add_u32 s84, s84, 0x100
	s_addc_u32 s85, s85, 0
	s_cmp_gt_u32 s86, 29
	s_barrier
	s_setprio 0
	s_cbranch_scc0 .LBB0_927
	s_and_b64 vcc, exec, s[14:15]
	s_cbranch_vccz .LBB0_930
	s_barrier

.LBB0_1171:
	s_add_i32 s95, s95, 2
	s_add_u32 s58, s58, 0x100
	s_addc_u32 s59, s59, 0
	s_add_u32 s92, s92, 0x100
	s_addc_u32 s93, s93, 0
	s_cmp_gt_u32 s95, 13
	s_barrier
	s_setprio 0
	s_cbranch_scc1 .LBB0_1180

.LBB0_1178:
	s_mov_b32 m0, s78
	v_lshl_add_u64 v[68:69], v[68:69], 0, s[44:45]
	s_add_u32 s60, s60, 0x40080
	global_load_lds_dwordx4 v[68:69], off
	v_lshl_add_u64 v[68:69], v[212:213], 0, s[44:45]
	s_mov_b32 m0, s79
	s_addc_u32 s61, s61, 0
	global_load_lds_dwordx4 v[68:69], off
	v_lshl_add_u64 v[68:69], s[60:61], 0, v[198:199]
	s_mov_b32 m0, s82
	s_and_b64 vcc, exec, s[6:7]
	global_load_lds_dwordx4 v[68:69], off
	v_lshl_add_u64 v[68:69], s[60:61], 0, v[204:205]
	s_mov_b32 m0, s83
	s_nop 0
	global_load_lds_dwordx4 v[68:69], off
	v_lshl_add_u64 v[68:69], v[214:215], 0, s[44:45]
	s_mov_b32 m0, s80
	s_nop 0
	global_load_lds_dwordx4 v[68:69], off
	v_lshl_add_u64 v[68:69], v[216:217], 0, s[44:45]
	s_mov_b32 m0, s81
	s_nop 0
	global_load_lds_dwordx4 v[68:69], off
	s_waitcnt vmcnt(8)
	s_waitcnt lgkmcnt(0)
	s_barrier
	s_cbranch_vccnz .LBB0_1171
	s_setprio 1
	s_waitcnt lgkmcnt(0)
	v_mfma_scale_f32_16x16x128_f8f6f4 v[130:133], v[18:25], v[34:41], v[130:133], v220, v220 op_sel_hi:[0,0,0]
	v_mfma_scale_f32_16x16x128_f8f6f4 v[122:125], v[26:33], v[34:41], v[122:125], v220, v220 op_sel_hi:[0,0,0]
	v_mfma_scale_f32_16x16x128_f8f6f4 v[114:117], v[18:25], v[42:49], v[114:117], v220, v220 op_sel_hi:[0,0,0]
	v_mfma_scale_f32_16x16x128_f8f6f4 v[106:109], v[26:33], v[42:49], v[106:109], v220, v220 op_sel_hi:[0,0,0]
	v_mfma_scale_f32_16x16x128_f8f6f4 v[98:101], v[18:25], v[50:57], v[98:101], v220, v220 op_sel_hi:[0,0,0]
	v_mfma_scale_f32_16x16x128_f8f6f4 v[90:93], v[26:33], v[50:57], v[90:93], v220, v220 op_sel_hi:[0,0,0]
	v_mfma_scale_f32_16x16x128_f8f6f4 v[82:85], v[18:25], v[58:65], v[82:85], v220, v220 op_sel_hi:[0,0,0]
	v_mfma_scale_f32_16x16x128_f8f6f4 v[74:77], v[26:33], v[58:65], v[74:77], v220, v220 op_sel_hi:[0,0,0]
	s_setprio 0
	s_setprio 1
	v_mfma_scale_f32_16x16x128_f8f6f4 v[126:129], v[2:9], v[34:41], v[126:129], v220, v220 op_sel_hi:[0,0,0]
	v_mfma_scale_f32_16x16x128_f8f6f4 v[118:121], v[10:17], v[34:41], v[118:121], v220, v220 op_sel_hi:[0,0,0]
	v_mfma_scale_f32_16x16x128_f8f6f4 v[110:113], v[2:9], v[42:49], v[110:113], v220, v220 op_sel_hi:[0,0,0]
	v_mfma_scale_f32_16x16x128_f8f6f4 v[102:105], v[10:17], v[42:49], v[102:105], v220, v220 op_sel_hi:[0,0,0]
	v_mfma_scale_f32_16x16x128_f8f6f4 v[94:97], v[2:9], v[50:57], v[94:97], v220, v220 op_sel_hi:[0,0,0]
	v_mfma_scale_f32_16x16x128_f8f6f4 v[86:89], v[10:17], v[50:57], v[86:89], v220, v220 op_sel_hi:[0,0,0]
	v_mfma_scale_f32_16x16x128_f8f6f4 v[78:81], v[2:9], v[58:65], v[78:81], v220, v220 op_sel_hi:[0,0,0]
	v_mfma_scale_f32_16x16x128_f8f6f4 v[70:73], v[10:17], v[58:65], v[70:73], v220, v220 op_sel_hi:[0,0,0]
	s_branch .LBB0_1171

.LBB0_1295:
	s_add_i32 s69, s69, 2
	s_add_u32 s64, s64, 0x100
	s_addc_u32 s65, s65, 0
	s_cmp_gt_u32 s69, 13
	v_lshl_add_u64 v[220:221], v[220:221], 0, s[52:53]
	s_barrier
	s_setprio 0
	s_cbranch_scc1 .LBB0_1304

.LBB0_1302:
	s_mov_b32 m0, s78
	v_lshl_add_u64 v[222:223], v[222:223], 0, s[46:47]
	global_load_lds_dwordx4 v[222:223], off
	v_lshl_add_u64 v[222:223], v[224:225], 0, s[46:47]
	s_mov_b32 m0, s79
	v_lshl_add_u64 v[68:69], v[68:69], 0, s[48:49]
	global_load_lds_dwordx4 v[222:223], off
	v_lshl_add_u64 v[222:223], v[68:69], 0, v[198:199]
	s_mov_b32 m0, s82
	v_lshl_add_u64 v[68:69], v[68:69], 0, v[206:207]
	global_load_lds_dwordx4 v[222:223], off
	s_mov_b32 m0, s83
	s_and_b64 vcc, exec, s[10:11]
	global_load_lds_dwordx4 v[68:69], off
	v_lshl_add_u64 v[68:69], v[226:227], 0, s[46:47]
	s_mov_b32 m0, s80
	s_nop 0
	global_load_lds_dwordx4 v[68:69], off
	v_lshl_add_u64 v[68:69], v[228:229], 0, s[46:47]
	s_mov_b32 m0, s81
	s_nop 0
	global_load_lds_dwordx4 v[68:69], off
	s_waitcnt vmcnt(8)
	s_waitcnt lgkmcnt(0)
	s_barrier
	s_cbranch_vccnz .LBB0_1295
	s_setprio 1
	s_waitcnt lgkmcnt(0)
	v_mfma_scale_f32_16x16x128_f8f6f4 v[130:133], v[18:25], v[34:41], v[130:133], v231, v231 op_sel_hi:[0,0,0]
	v_mfma_scale_f32_16x16x128_f8f6f4 v[126:129], v[26:33], v[34:41], v[126:129], v231, v231 op_sel_hi:[0,0,0]
	v_mfma_scale_f32_16x16x128_f8f6f4 v[122:125], v[18:25], v[42:49], v[122:125], v231, v231 op_sel_hi:[0,0,0]
	v_mfma_scale_f32_16x16x128_f8f6f4 v[118:121], v[26:33], v[42:49], v[118:121], v231, v231 op_sel_hi:[0,0,0]
	v_mfma_scale_f32_16x16x128_f8f6f4 v[98:101], v[18:25], v[50:57], v[98:101], v231, v231 op_sel_hi:[0,0,0]
	v_mfma_scale_f32_16x16x128_f8f6f4 v[94:97], v[26:33], v[50:57], v[94:97], v231, v231 op_sel_hi:[0,0,0]
	v_mfma_scale_f32_16x16x128_f8f6f4 v[90:93], v[18:25], v[58:65], v[90:93], v231, v231 op_sel_hi:[0,0,0]
	v_mfma_scale_f32_16x16x128_f8f6f4 v[86:89], v[26:33], v[58:65], v[86:89], v231, v231 op_sel_hi:[0,0,0]
	s_setprio 0
	s_setprio 1
	v_mfma_scale_f32_16x16x128_f8f6f4 v[114:117], v[2:9], v[34:41], v[114:117], v231, v231 op_sel_hi:[0,0,0]
	v_mfma_scale_f32_16x16x128_f8f6f4 v[110:113], v[10:17], v[34:41], v[110:113], v231, v231 op_sel_hi:[0,0,0]
	v_mfma_scale_f32_16x16x128_f8f6f4 v[106:109], v[2:9], v[42:49], v[106:109], v231, v231 op_sel_hi:[0,0,0]
	v_mfma_scale_f32_16x16x128_f8f6f4 v[102:105], v[10:17], v[42:49], v[102:105], v231, v231 op_sel_hi:[0,0,0]
	v_mfma_scale_f32_16x16x128_f8f6f4 v[82:85], v[2:9], v[50:57], v[82:85], v231, v231 op_sel_hi:[0,0,0]
	v_mfma_scale_f32_16x16x128_f8f6f4 v[78:81], v[10:17], v[50:57], v[78:81], v231, v231 op_sel_hi:[0,0,0]
	v_mfma_scale_f32_16x16x128_f8f6f4 v[74:77], v[2:9], v[58:65], v[74:77], v231, v231 op_sel_hi:[0,0,0]
	v_mfma_scale_f32_16x16x128_f8f6f4 v[70:73], v[10:17], v[58:65], v[70:73], v231, v231 op_sel_hi:[0,0,0]
	s_branch .LBB0_1295
